# P2 expert-weight conversion rewritten by hand (no LDS transpose: loads remapped so cvt_pk packs along k; ring of 6 items per wave, 2 conversion waves instead of 3)
# baseline (speedup 1.0000x reference)
.LBB0_416:
	s_cmp_lt_i32 s80, 3
	s_cselect_b64 s[4:5], -1, 0
	s_add_u32 s2, s90, 0x1800000
	s_addc_u32 s3, s91, 0
	s_add_u32 s66, s90, 0x5800000
	s_addc_u32 s67, s91, 0
	s_add_u32 s6, s90, 0x1b000000
	s_addc_u32 s7, s91, 0
	v_writelane_b32 v255, s6, 50
	s_and_b64 s[4:5], s[4:5], s[0:1]
	s_mov_b32 s19, 0
	v_writelane_b32 v255, s7, 51
	s_mov_b32 s6, 1
	s_cmp_gt_i32 s6, 0
	s_cselect_b64 s[0:1], -1, 0
	s_and_b64 s[0:1], s[4:5], s[0:1]
	v_writelane_b32 v255, s6, 43
	s_andn2_b64 vcc, exec, s[0:1]
	s_cbranch_vccnz .LBB0_819
	v_writelane_b32 v255, s4, 52
	s_add_u32 s10, s90, 0x1e000000
	s_addc_u32 s11, s91, 0
	v_writelane_b32 v255, s5, 53
	s_add_u32 s14, s90, 0x15800000
	v_readlane_b32 s0, v255, 2
	s_addc_u32 s15, s91, 0
	s_addk_i32 s0, 0x7ff
	s_ashr_i32 s1, s0, 31
	v_readlane_b32 s4, v255, 19
	s_abs_i32 s0, s0
	s_xor_b32 s1, s1, s4
	s_mul_hi_u32 s4, s0, s96
	s_mul_i32 s5, s4, s94
	s_sub_i32 s0, s0, s5
	s_add_i32 s5, s4, 1
	s_sub_i32 s6, s0, s94
	s_cmp_ge_u32 s0, s94
	s_cselect_b32 s4, s5, s4
	s_cselect_b32 s0, s6, s0
	s_add_i32 s5, s4, 1
	s_cmp_ge_u32 s0, s94
	s_cselect_b32 s0, s5, s4
	s_xor_b32 s0, s0, s1
	s_sub_i32 s35, s0, s1
	v_readlane_b32 s0, v255, 18
	v_readlane_b32 s7, v255, 20
	s_mulk_i32 s0, 0x2100
	s_add_i32 s79, s35, s33
	s_add_i32 s9, s7, s33
	s_add_i32 s0, s0, 0
	s_cmp_gt_i32 s79, 0
	s_cselect_b64 s[4:5], -1, 0
	v_writelane_b32 v255, s4, 41
	v_lshrrev_b32_e32 v142, 3, v1
	s_waitcnt vmcnt(0)
	v_and_b32_e32 v4, 7, v0
	v_writelane_b32 v255, s5, 42
	v_mul_u32_u24_e32 v2, 0x84, v142
	v_readlane_b32 s1, v255, 27
	v_readlane_b32 s6, v255, 8
	s_cmpk_lt_u32 s1, 0x180
	s_mul_i32 s1, s7, s6
	s_cselect_b64 s[82:83], -1, 0
	s_sub_i32 s22, s1, s33
	v_lshlrev_b32_e32 v5, 4, v4
	s_mul_i32 s23, s33, s6
	s_add_u32 s84, s90, 0xe00400
	v_add3_u32 v143, s0, v2, v5
	v_lshlrev_b32_e32 v146, 3, v4
	v_mul_u32_u24_e32 v2, 0x420, v4
	v_lshlrev_b32_e32 v4, 2, v142
	s_addc_u32 s85, s91, 0
	v_add3_u32 v145, s0, v2, v4
	s_sub_i32 s0, s23, s35
	v_writelane_b32 v255, s0, 58
	s_mul_i32 s0, s35, s6
	s_addk_i32 s0, 0x1000
	v_writelane_b32 v255, s0, 57
	v_writelane_b32 v255, s14, 39
	v_mov_b32_e32 v3, 0
	v_and_b32_e32 v149, 15, v0
	v_writelane_b32 v255, s15, 40
	v_lshlrev_b32_e32 v160, 6, v149
	v_mov_b32_e32 v161, v3
	v_writelane_b32 v255, s10, 60
	v_and_b32_e32 v2, 48, v1
	v_and_b32_e32 v154, 48, v0
	v_writelane_b32 v255, s11, 61
	v_lshl_add_u64 v[4:5], s[10:11], 0, v[160:161]
	v_lshl_add_u64 v[164:165], v[4:5], 0, v[2:3]
	v_lshrrev_b32_e32 v4, 2, v0
	v_readlane_b32 s0, v255, 31
	v_mov_b32_e32 v155, v3
	v_and_b32_e32 v166, 12, v4
	v_readlane_b32 s1, v255, 32
	v_lshl_add_u64 v[4:5], s[90:91], 0, v[160:161]
	v_lshlrev_b32_e32 v151, 4, v149
	v_lshl_add_u64 v[168:169], s[0:1], 0, v[154:155]
	v_lshl_add_u64 v[4:5], v[4:5], 0, v[2:3]
	s_mov_b64 s[0:1], 0x1d800000
	v_lshl_add_u64 v[170:171], v[4:5], 0, s[0:1]
	v_sub_u32_e32 v4, v2, v160
	v_sub_u32_e32 v2, v2, v151
	s_add_i32 s0, 0, 0x20280
	v_lshlrev_b32_e32 v6, 2, v0
	v_lshrrev_b32_e32 v7, 4, v1
	v_add_u32_e32 v2, 0, v2
	v_writelane_b32 v255, s0, 48
	s_mov_b32 s0, 0
	v_lshlrev_b32_e32 v153, 2, v7
	v_cmp_gt_u32_e32 vcc, 16, v1
	v_add_u32_e32 v161, 0, v6
	v_add_u32_e32 v4, 0, v4
	v_add_u32_e32 v182, 0x7c50, v2
	v_mbcnt_lo_u32_b32 v2, -1, 0
	v_writelane_b32 v255, s0, 14
	v_cmp_eq_u32_e64 s[4:5], 0, v1
	v_and_b32_e32 v144, 28, v6
	v_mov_b32_e32 v147, v3
	v_or_b32_e32 v148, 8, v142
	v_or_b32_e32 v150, 16, v142
	v_or_b32_e32 v152, 24, v142
	v_lshl_add_u64 v[156:157], s[14:15], 0, v[154:155]
	v_lshlrev_b32_e32 v158, 5, v149
	v_lshlrev_b32_e32 v162, 3, v7
	v_lshlrev_b32_e32 v159, 2, v149
	v_mov_b32_e32 v167, v3
	v_cndmask_b32_e64 v163, 0, 1.0, vcc
	v_add_u32_e32 v180, 0x5040, v161
	v_add_u32_e32 v181, 0x5420, v4
	v_sub_u32_e32 v183, v153, v149
	s_add_i32 s14, 0, 0x20284
	v_mov_b32_e32 v184, 0xff
	v_mbcnt_hi_u32_b32 v185, -1, v2
	v_mov_b32_e32 v186, 0x1e00000
	v_writelane_b32 v255, s35, 44
	s_branch .LBB0_420

.LBB0_436:
	s_xor_b64 s[6:7], s[88:89], -1
	s_and_b64 s[10:11], s[82:83], s[90:91]
	s_or_b64 s[6:7], s[6:7], s[10:11]
	s_mov_b64 s[0:1], -1
	s_and_b64 vcc, exec, s[6:7]
	s_cbranch_vccnz .LBB0_634
	s_mov_b32 s30, 0x42000000
	v_lshrrev_b32_e32 v133, 3, v1
	v_and_b32_e32 v134, 7, v1
	v_lshlrev_b32_e32 v135, 15, v133
	v_lshl_add_u32 v132, v134, 4, v135
	v_lshlrev_b32_e32 v140, 12, v134
	v_lshl_add_u32 v140, v133, 3, v140
	v_add_u32_e32 v133, 0x1000, v132
	v_add_u32_e32 v134, 0x2000, v132
	v_add_u32_e32 v135, 0x3000, v132
	v_add_u32_e32 v136, 0x4000, v132
	v_add_u32_e32 v137, 0x5000, v132
	v_add_u32_e32 v138, 0x6000, v132
	v_add_u32_e32 v139, 0x7000, v132
	v_mov_b32_e32 v141, s14
	v_mov_b32_e32 v187, 1
	s_mov_b32 s28, 0
	s_mov_b32 s29, 0
.Lcv2_loop:
	s_bitcmp1_b32 s29, 0
	s_cbranch_scc0 .Lcv2_t0
	s_sub_u32 s0, s28, s60
	s_cmp_lt_u32 s0, 60
	s_cbranch_scc1 .Lcv2_slow0
	s_waitcnt vmcnt(60)
.Lcv2_go0:
	v_pk_mul_f32 v[4:5], v[4:5], s[30:31] op_sel_hi:[1,0]
	v_pk_mul_f32 v[6:7], v[6:7], s[30:31] op_sel_hi:[1,0]
	v_pk_mul_f32 v[8:9], v[8:9], s[30:31] op_sel_hi:[1,0]
	v_pk_mul_f32 v[10:11], v[10:11], s[30:31] op_sel_hi:[1,0]
	v_pk_mul_f32 v[12:13], v[12:13], s[30:31] op_sel_hi:[1,0]
	v_pk_mul_f32 v[14:15], v[14:15], s[30:31] op_sel_hi:[1,0]
	v_pk_mul_f32 v[16:17], v[16:17], s[30:31] op_sel_hi:[1,0]
	v_pk_mul_f32 v[18:19], v[18:19], s[30:31] op_sel_hi:[1,0]
	v_pk_mul_f32 v[20:21], v[20:21], s[30:31] op_sel_hi:[1,0]
	v_pk_mul_f32 v[22:23], v[22:23], s[30:31] op_sel_hi:[1,0]
	v_pk_mul_f32 v[24:25], v[24:25], s[30:31] op_sel_hi:[1,0]
	v_pk_mul_f32 v[26:27], v[26:27], s[30:31] op_sel_hi:[1,0]
	v_pk_mul_f32 v[28:29], v[28:29], s[30:31] op_sel_hi:[1,0]
	v_pk_mul_f32 v[30:31], v[30:31], s[30:31] op_sel_hi:[1,0]
	v_pk_mul_f32 v[32:33], v[32:33], s[30:31] op_sel_hi:[1,0]
	v_pk_mul_f32 v[34:35], v[34:35], s[30:31] op_sel_hi:[1,0]
	v_cvt_pk_fp8_f32 v172, v4, v8
	v_cvt_pk_fp8_f32 v174, v5, v9
	v_cvt_pk_fp8_f32 v173, v20, v24
	v_cvt_pk_fp8_f32 v175, v21, v25
	v_cvt_pk_fp8_f32 v172, v12, v16 op_sel:[0,0,1]
	v_cvt_pk_fp8_f32 v174, v13, v17 op_sel:[0,0,1]
	v_cvt_pk_fp8_f32 v173, v28, v32 op_sel:[0,0,1]
	v_cvt_pk_fp8_f32 v175, v29, v33 op_sel:[0,0,1]
	v_cvt_pk_fp8_f32 v176, v6, v10
	v_cvt_pk_fp8_f32 v178, v7, v11
	v_cvt_pk_fp8_f32 v177, v22, v26
	v_cvt_pk_fp8_f32 v179, v23, v27
	v_cvt_pk_fp8_f32 v176, v14, v18 op_sel:[0,0,1]
	v_cvt_pk_fp8_f32 v178, v15, v19 op_sel:[0,0,1]
	v_cvt_pk_fp8_f32 v177, v30, v34 op_sel:[0,0,1]
	v_cvt_pk_fp8_f32 v179, v31, v35 op_sel:[0,0,1]
	s_add_u32 s28, s28, 4
	s_bitset0_b32 s29, 0
	global_store_dwordx2 v140, v[172:173], s[68:69] nt
	global_store_dwordx2 v140, v[174:175], s[68:69] offset:1024 nt
	global_store_dwordx2 v140, v[176:177], s[68:69] offset:2048 nt
	global_store_dwordx2 v140, v[178:179], s[68:69] offset:3072 nt
.Lcv2_t0:
	s_bitcmp1_b32 s29, 31
	s_cbranch_scc1 .Lcv2_n0
	s_mov_b64 exec, s[4:5]
	ds_add_rtn_u32 v2, v141, v187
	s_mov_b64 exec, -1
	s_waitcnt lgkmcnt(0)
	v_readfirstlane_b32 s0, v2
	s_cmp_ge_i32 s0, s9
	s_cbranch_scc1 .Lcv2_e0
	s_add_i32 s0, s22, s0
	s_min_i32 s0, s0, 0xbfff
	s_lshr_b32 s1, s0, 9
	s_mul_i32 s6, s1, 0xab
	s_lshr_b32 s6, s6, 9
	s_mul_i32 s7, s6, 3
	s_sub_i32 s1, s1, s7
	s_and_b32 s0, s0, 0x1ff
	s_lshr_b32 s7, s0, 5
	s_and_b32 s0, s0, 31
	s_lshl_b32 s8, s6, 22
	s_lshl_b32 s10, s7, 18
	s_add_u32 s8, s8, s10
	s_lshl_b32 s10, s0, 7
	s_add_u32 s8, s8, s10
	s_cmp_eq_u32 s1, 0
	s_cselect_b64 s[10:11], s[44:45], s[48:49]
	s_cmp_eq_u32 s1, 2
	s_cselect_b64 s[10:11], s[52:53], s[10:11]
	s_add_u32 s10, s10, s8
	s_addc_u32 s11, s11, 0
	s_lshl_b32 s7, s7, 6
	s_lshl_b32 s8, s6, 20
	s_lshl_b32 s15, s0, 15
	s_add_u32 s8, s8, s15
	s_lshl_b32 s6, s6, 21
	s_lshr_b32 s15, s0, 2
	s_lshl_b32 s15, s15, 18
	s_add_u32 s6, s6, s15
	s_lshl_b32 s15, s1, 17
	s_add_u32 s6, s6, s15
	s_and_b32 s15, s0, 3
	s_lshl_b32 s15, s15, 15
	s_add_u32 s6, s6, s15
	s_cmp_eq_u32 s1, 2
	s_cselect_b32 s6, s8, s6
	s_cselect_b64 s[68:69], s[66:67], s[2:3]
	s_add_u32 s6, s6, s7
	s_add_u32 s68, s68, s6
	s_addc_u32 s69, s69, 0
	global_load_dwordx4 v[4:7], v132, s[10:11] nt
	global_load_dwordx4 v[8:11], v133, s[10:11] nt
	global_load_dwordx4 v[12:15], v134, s[10:11] nt
	global_load_dwordx4 v[16:19], v135, s[10:11] nt
	global_load_dwordx4 v[20:23], v136, s[10:11] nt
	global_load_dwordx4 v[24:27], v137, s[10:11] nt
	global_load_dwordx4 v[28:31], v138, s[10:11] nt
	global_load_dwordx4 v[32:35], v139, s[10:11] nt
	s_add_u32 s28, s28, 8
	s_mov_b32 s60, s28
	s_bitset1_b32 s29, 0
.Lcv2_n0:
	s_bitcmp1_b32 s29, 1
	s_cbranch_scc0 .Lcv2_t1
	s_sub_u32 s0, s28, s61
	s_cmp_lt_u32 s0, 60
	s_cbranch_scc1 .Lcv2_slow1
	s_waitcnt vmcnt(60)
.Lcv2_go1:
	v_pk_mul_f32 v[36:37], v[36:37], s[30:31] op_sel_hi:[1,0]
	v_pk_mul_f32 v[38:39], v[38:39], s[30:31] op_sel_hi:[1,0]
	v_pk_mul_f32 v[40:41], v[40:41], s[30:31] op_sel_hi:[1,0]
	v_pk_mul_f32 v[42:43], v[42:43], s[30:31] op_sel_hi:[1,0]
	v_pk_mul_f32 v[44:45], v[44:45], s[30:31] op_sel_hi:[1,0]
	v_pk_mul_f32 v[46:47], v[46:47], s[30:31] op_sel_hi:[1,0]
	v_pk_mul_f32 v[48:49], v[48:49], s[30:31] op_sel_hi:[1,0]
	v_pk_mul_f32 v[50:51], v[50:51], s[30:31] op_sel_hi:[1,0]
	v_pk_mul_f32 v[52:53], v[52:53], s[30:31] op_sel_hi:[1,0]
	v_pk_mul_f32 v[54:55], v[54:55], s[30:31] op_sel_hi:[1,0]
	v_pk_mul_f32 v[56:57], v[56:57], s[30:31] op_sel_hi:[1,0]
	v_pk_mul_f32 v[58:59], v[58:59], s[30:31] op_sel_hi:[1,0]
	v_pk_mul_f32 v[60:61], v[60:61], s[30:31] op_sel_hi:[1,0]
	v_pk_mul_f32 v[62:63], v[62:63], s[30:31] op_sel_hi:[1,0]
	v_pk_mul_f32 v[64:65], v[64:65], s[30:31] op_sel_hi:[1,0]
	v_pk_mul_f32 v[66:67], v[66:67], s[30:31] op_sel_hi:[1,0]
	v_cvt_pk_fp8_f32 v172, v36, v40
	v_cvt_pk_fp8_f32 v174, v37, v41
	v_cvt_pk_fp8_f32 v173, v52, v56
	v_cvt_pk_fp8_f32 v175, v53, v57
	v_cvt_pk_fp8_f32 v172, v44, v48 op_sel:[0,0,1]
	v_cvt_pk_fp8_f32 v174, v45, v49 op_sel:[0,0,1]
	v_cvt_pk_fp8_f32 v173, v60, v64 op_sel:[0,0,1]
	v_cvt_pk_fp8_f32 v175, v61, v65 op_sel:[0,0,1]
	v_cvt_pk_fp8_f32 v176, v38, v42
	v_cvt_pk_fp8_f32 v178, v39, v43
	v_cvt_pk_fp8_f32 v177, v54, v58
	v_cvt_pk_fp8_f32 v179, v55, v59
	v_cvt_pk_fp8_f32 v176, v46, v50 op_sel:[0,0,1]
	v_cvt_pk_fp8_f32 v178, v47, v51 op_sel:[0,0,1]
	v_cvt_pk_fp8_f32 v177, v62, v66 op_sel:[0,0,1]
	v_cvt_pk_fp8_f32 v179, v63, v67 op_sel:[0,0,1]
	s_add_u32 s28, s28, 4
	s_bitset0_b32 s29, 1
	global_store_dwordx2 v140, v[172:173], s[76:77] nt
	global_store_dwordx2 v140, v[174:175], s[76:77] offset:1024 nt
	global_store_dwordx2 v140, v[176:177], s[76:77] offset:2048 nt
	global_store_dwordx2 v140, v[178:179], s[76:77] offset:3072 nt
.Lcv2_t1:
	s_bitcmp1_b32 s29, 31
	s_cbranch_scc1 .Lcv2_n1
	s_mov_b64 exec, s[4:5]
	ds_add_rtn_u32 v2, v141, v187
	s_mov_b64 exec, -1
	s_waitcnt lgkmcnt(0)
	v_readfirstlane_b32 s0, v2
	s_cmp_ge_i32 s0, s9
	s_cbranch_scc1 .Lcv2_e1
	s_add_i32 s0, s22, s0
	s_min_i32 s0, s0, 0xbfff
	s_lshr_b32 s1, s0, 9
	s_mul_i32 s6, s1, 0xab
	s_lshr_b32 s6, s6, 9
	s_mul_i32 s7, s6, 3
	s_sub_i32 s1, s1, s7
	s_and_b32 s0, s0, 0x1ff
	s_lshr_b32 s7, s0, 5
	s_and_b32 s0, s0, 31
	s_lshl_b32 s8, s6, 22
	s_lshl_b32 s10, s7, 18
	s_add_u32 s8, s8, s10
	s_lshl_b32 s10, s0, 7
	s_add_u32 s8, s8, s10
	s_cmp_eq_u32 s1, 0
	s_cselect_b64 s[10:11], s[44:45], s[48:49]
	s_cmp_eq_u32 s1, 2
	s_cselect_b64 s[10:11], s[52:53], s[10:11]
	s_add_u32 s10, s10, s8
	s_addc_u32 s11, s11, 0
	s_lshl_b32 s7, s7, 6
	s_lshl_b32 s8, s6, 20
	s_lshl_b32 s15, s0, 15
	s_add_u32 s8, s8, s15
	s_lshl_b32 s6, s6, 21
	s_lshr_b32 s15, s0, 2
	s_lshl_b32 s15, s15, 18
	s_add_u32 s6, s6, s15
	s_lshl_b32 s15, s1, 17
	s_add_u32 s6, s6, s15
	s_and_b32 s15, s0, 3
	s_lshl_b32 s15, s15, 15
	s_add_u32 s6, s6, s15
	s_cmp_eq_u32 s1, 2
	s_cselect_b32 s6, s8, s6
	s_cselect_b64 s[76:77], s[66:67], s[2:3]
	s_add_u32 s6, s6, s7
	s_add_u32 s76, s76, s6
	s_addc_u32 s77, s77, 0
	global_load_dwordx4 v[36:39], v132, s[10:11] nt
	global_load_dwordx4 v[40:43], v133, s[10:11] nt
	global_load_dwordx4 v[44:47], v134, s[10:11] nt
	global_load_dwordx4 v[48:51], v135, s[10:11] nt
	global_load_dwordx4 v[52:55], v136, s[10:11] nt
	global_load_dwordx4 v[56:59], v137, s[10:11] nt
	global_load_dwordx4 v[60:63], v138, s[10:11] nt
	global_load_dwordx4 v[64:67], v139, s[10:11] nt
	s_add_u32 s28, s28, 8
	s_mov_b32 s61, s28
	s_bitset1_b32 s29, 1
.Lcv2_n1:
	s_bitcmp1_b32 s29, 2
	s_cbranch_scc0 .Lcv2_t2
	s_sub_u32 s0, s28, s62
	s_cmp_lt_u32 s0, 60
	s_cbranch_scc1 .Lcv2_slow2
	s_waitcnt vmcnt(60)
.Lcv2_go2:
	v_pk_mul_f32 v[68:69], v[68:69], s[30:31] op_sel_hi:[1,0]
	v_pk_mul_f32 v[70:71], v[70:71], s[30:31] op_sel_hi:[1,0]
	v_pk_mul_f32 v[72:73], v[72:73], s[30:31] op_sel_hi:[1,0]
	v_pk_mul_f32 v[74:75], v[74:75], s[30:31] op_sel_hi:[1,0]
	v_pk_mul_f32 v[76:77], v[76:77], s[30:31] op_sel_hi:[1,0]
	v_pk_mul_f32 v[78:79], v[78:79], s[30:31] op_sel_hi:[1,0]
	v_pk_mul_f32 v[80:81], v[80:81], s[30:31] op_sel_hi:[1,0]
	v_pk_mul_f32 v[82:83], v[82:83], s[30:31] op_sel_hi:[1,0]
	v_pk_mul_f32 v[84:85], v[84:85], s[30:31] op_sel_hi:[1,0]
	v_pk_mul_f32 v[86:87], v[86:87], s[30:31] op_sel_hi:[1,0]
	v_pk_mul_f32 v[88:89], v[88:89], s[30:31] op_sel_hi:[1,0]
	v_pk_mul_f32 v[90:91], v[90:91], s[30:31] op_sel_hi:[1,0]
	v_pk_mul_f32 v[92:93], v[92:93], s[30:31] op_sel_hi:[1,0]
	v_pk_mul_f32 v[94:95], v[94:95], s[30:31] op_sel_hi:[1,0]
	v_pk_mul_f32 v[96:97], v[96:97], s[30:31] op_sel_hi:[1,0]
	v_pk_mul_f32 v[98:99], v[98:99], s[30:31] op_sel_hi:[1,0]
	v_cvt_pk_fp8_f32 v172, v68, v72
	v_cvt_pk_fp8_f32 v174, v69, v73
	v_cvt_pk_fp8_f32 v173, v84, v88
	v_cvt_pk_fp8_f32 v175, v85, v89
	v_cvt_pk_fp8_f32 v172, v76, v80 op_sel:[0,0,1]
	v_cvt_pk_fp8_f32 v174, v77, v81 op_sel:[0,0,1]
	v_cvt_pk_fp8_f32 v173, v92, v96 op_sel:[0,0,1]
	v_cvt_pk_fp8_f32 v175, v93, v97 op_sel:[0,0,1]
	v_cvt_pk_fp8_f32 v176, v70, v74
	v_cvt_pk_fp8_f32 v178, v71, v75
	v_cvt_pk_fp8_f32 v177, v86, v90
	v_cvt_pk_fp8_f32 v179, v87, v91
	v_cvt_pk_fp8_f32 v176, v78, v82 op_sel:[0,0,1]
	v_cvt_pk_fp8_f32 v178, v79, v83 op_sel:[0,0,1]
	v_cvt_pk_fp8_f32 v177, v94, v98 op_sel:[0,0,1]
	v_cvt_pk_fp8_f32 v179, v95, v99 op_sel:[0,0,1]
	s_add_u32 s28, s28, 4
	s_bitset0_b32 s29, 2
	global_store_dwordx2 v140, v[172:173], s[80:81] nt
	global_store_dwordx2 v140, v[174:175], s[80:81] offset:1024 nt
	global_store_dwordx2 v140, v[176:177], s[80:81] offset:2048 nt
	global_store_dwordx2 v140, v[178:179], s[80:81] offset:3072 nt
.Lcv2_t2:
	s_bitcmp1_b32 s29, 31
	s_cbranch_scc1 .Lcv2_n2
	s_mov_b64 exec, s[4:5]
	ds_add_rtn_u32 v2, v141, v187
	s_mov_b64 exec, -1
	s_waitcnt lgkmcnt(0)
	v_readfirstlane_b32 s0, v2
	s_cmp_ge_i32 s0, s9
	s_cbranch_scc1 .Lcv2_e2
	s_add_i32 s0, s22, s0
	s_min_i32 s0, s0, 0xbfff
	s_lshr_b32 s1, s0, 9
	s_mul_i32 s6, s1, 0xab
	s_lshr_b32 s6, s6, 9
	s_mul_i32 s7, s6, 3
	s_sub_i32 s1, s1, s7
	s_and_b32 s0, s0, 0x1ff
	s_lshr_b32 s7, s0, 5
	s_and_b32 s0, s0, 31
	s_lshl_b32 s8, s6, 22
	s_lshl_b32 s10, s7, 18
	s_add_u32 s8, s8, s10
	s_lshl_b32 s10, s0, 7
	s_add_u32 s8, s8, s10
	s_cmp_eq_u32 s1, 0
	s_cselect_b64 s[10:11], s[44:45], s[48:49]
	s_cmp_eq_u32 s1, 2
	s_cselect_b64 s[10:11], s[52:53], s[10:11]
	s_add_u32 s10, s10, s8
	s_addc_u32 s11, s11, 0
	s_lshl_b32 s7, s7, 6
	s_lshl_b32 s8, s6, 20
	s_lshl_b32 s15, s0, 15
	s_add_u32 s8, s8, s15
	s_lshl_b32 s6, s6, 21
	s_lshr_b32 s15, s0, 2
	s_lshl_b32 s15, s15, 18
	s_add_u32 s6, s6, s15
	s_lshl_b32 s15, s1, 17
	s_add_u32 s6, s6, s15
	s_and_b32 s15, s0, 3
	s_lshl_b32 s15, s15, 15
	s_add_u32 s6, s6, s15
	s_cmp_eq_u32 s1, 2
	s_cselect_b32 s6, s8, s6
	s_cselect_b64 s[80:81], s[66:67], s[2:3]
	s_add_u32 s6, s6, s7
	s_add_u32 s80, s80, s6
	s_addc_u32 s81, s81, 0
	global_load_dwordx4 v[68:71], v132, s[10:11] nt
	global_load_dwordx4 v[72:75], v133, s[10:11] nt
	global_load_dwordx4 v[76:79], v134, s[10:11] nt
	global_load_dwordx4 v[80:83], v135, s[10:11] nt
	global_load_dwordx4 v[84:87], v136, s[10:11] nt
	global_load_dwordx4 v[88:91], v137, s[10:11] nt
	global_load_dwordx4 v[92:95], v138, s[10:11] nt
	global_load_dwordx4 v[96:99], v139, s[10:11] nt
	s_add_u32 s28, s28, 8
	s_mov_b32 s62, s28
	s_bitset1_b32 s29, 2
.Lcv2_n2:
	s_bitcmp1_b32 s29, 3
	s_cbranch_scc0 .Lcv2_t3
	s_sub_u32 s0, s28, s63
	s_cmp_lt_u32 s0, 60
	s_cbranch_scc1 .Lcv2_slow3
	s_waitcnt vmcnt(60)
.Lcv2_go3:
	v_pk_mul_f32 v[100:101], v[100:101], s[30:31] op_sel_hi:[1,0]
	v_pk_mul_f32 v[102:103], v[102:103], s[30:31] op_sel_hi:[1,0]
	v_pk_mul_f32 v[104:105], v[104:105], s[30:31] op_sel_hi:[1,0]
	v_pk_mul_f32 v[106:107], v[106:107], s[30:31] op_sel_hi:[1,0]
	v_pk_mul_f32 v[108:109], v[108:109], s[30:31] op_sel_hi:[1,0]
	v_pk_mul_f32 v[110:111], v[110:111], s[30:31] op_sel_hi:[1,0]
	v_pk_mul_f32 v[112:113], v[112:113], s[30:31] op_sel_hi:[1,0]
	v_pk_mul_f32 v[114:115], v[114:115], s[30:31] op_sel_hi:[1,0]
	v_pk_mul_f32 v[116:117], v[116:117], s[30:31] op_sel_hi:[1,0]
	v_pk_mul_f32 v[118:119], v[118:119], s[30:31] op_sel_hi:[1,0]
	v_pk_mul_f32 v[120:121], v[120:121], s[30:31] op_sel_hi:[1,0]
	v_pk_mul_f32 v[122:123], v[122:123], s[30:31] op_sel_hi:[1,0]
	v_pk_mul_f32 v[124:125], v[124:125], s[30:31] op_sel_hi:[1,0]
	v_pk_mul_f32 v[126:127], v[126:127], s[30:31] op_sel_hi:[1,0]
	v_pk_mul_f32 v[128:129], v[128:129], s[30:31] op_sel_hi:[1,0]
	v_pk_mul_f32 v[130:131], v[130:131], s[30:31] op_sel_hi:[1,0]
	v_cvt_pk_fp8_f32 v172, v100, v104
	v_cvt_pk_fp8_f32 v174, v101, v105
	v_cvt_pk_fp8_f32 v173, v116, v120
	v_cvt_pk_fp8_f32 v175, v117, v121
	v_cvt_pk_fp8_f32 v172, v108, v112 op_sel:[0,0,1]
	v_cvt_pk_fp8_f32 v174, v109, v113 op_sel:[0,0,1]
	v_cvt_pk_fp8_f32 v173, v124, v128 op_sel:[0,0,1]
	v_cvt_pk_fp8_f32 v175, v125, v129 op_sel:[0,0,1]
	v_cvt_pk_fp8_f32 v176, v102, v106
	v_cvt_pk_fp8_f32 v178, v103, v107
	v_cvt_pk_fp8_f32 v177, v118, v122
	v_cvt_pk_fp8_f32 v179, v119, v123
	v_cvt_pk_fp8_f32 v176, v110, v114 op_sel:[0,0,1]
	v_cvt_pk_fp8_f32 v178, v111, v115 op_sel:[0,0,1]
	v_cvt_pk_fp8_f32 v177, v126, v130 op_sel:[0,0,1]
	v_cvt_pk_fp8_f32 v179, v127, v131 op_sel:[0,0,1]
	s_add_u32 s28, s28, 4
	s_bitset0_b32 s29, 3
	global_store_dwordx2 v140, v[172:173], s[86:87] nt
	global_store_dwordx2 v140, v[174:175], s[86:87] offset:1024 nt
	global_store_dwordx2 v140, v[176:177], s[86:87] offset:2048 nt
	global_store_dwordx2 v140, v[178:179], s[86:87] offset:3072 nt
.Lcv2_t3:
	s_bitcmp1_b32 s29, 31
	s_cbranch_scc1 .Lcv2_n3
	s_mov_b64 exec, s[4:5]
	ds_add_rtn_u32 v2, v141, v187
	s_mov_b64 exec, -1
	s_waitcnt lgkmcnt(0)
	v_readfirstlane_b32 s0, v2
	s_cmp_ge_i32 s0, s9
	s_cbranch_scc1 .Lcv2_e3
	s_add_i32 s0, s22, s0
	s_min_i32 s0, s0, 0xbfff
	s_lshr_b32 s1, s0, 9
	s_mul_i32 s6, s1, 0xab
	s_lshr_b32 s6, s6, 9
	s_mul_i32 s7, s6, 3
	s_sub_i32 s1, s1, s7
	s_and_b32 s0, s0, 0x1ff
	s_lshr_b32 s7, s0, 5
	s_and_b32 s0, s0, 31
	s_lshl_b32 s8, s6, 22
	s_lshl_b32 s10, s7, 18
	s_add_u32 s8, s8, s10
	s_lshl_b32 s10, s0, 7
	s_add_u32 s8, s8, s10
	s_cmp_eq_u32 s1, 0
	s_cselect_b64 s[10:11], s[44:45], s[48:49]
	s_cmp_eq_u32 s1, 2
	s_cselect_b64 s[10:11], s[52:53], s[10:11]
	s_add_u32 s10, s10, s8
	s_addc_u32 s11, s11, 0
	s_lshl_b32 s7, s7, 6
	s_lshl_b32 s8, s6, 20
	s_lshl_b32 s15, s0, 15
	s_add_u32 s8, s8, s15
	s_lshl_b32 s6, s6, 21
	s_lshr_b32 s15, s0, 2
	s_lshl_b32 s15, s15, 18
	s_add_u32 s6, s6, s15
	s_lshl_b32 s15, s1, 17
	s_add_u32 s6, s6, s15
	s_and_b32 s15, s0, 3
	s_lshl_b32 s15, s15, 15
	s_add_u32 s6, s6, s15
	s_cmp_eq_u32 s1, 2
	s_cselect_b32 s6, s8, s6
	s_cselect_b64 s[86:87], s[66:67], s[2:3]
	s_add_u32 s6, s6, s7
	s_add_u32 s86, s86, s6
	s_addc_u32 s87, s87, 0
	global_load_dwordx4 v[100:103], v132, s[10:11] nt
	global_load_dwordx4 v[104:107], v133, s[10:11] nt
	global_load_dwordx4 v[108:111], v134, s[10:11] nt
	global_load_dwordx4 v[112:115], v135, s[10:11] nt
	global_load_dwordx4 v[116:119], v136, s[10:11] nt
	global_load_dwordx4 v[120:123], v137, s[10:11] nt
	global_load_dwordx4 v[124:127], v138, s[10:11] nt
	global_load_dwordx4 v[128:131], v139, s[10:11] nt
	s_add_u32 s28, s28, 8
	s_mov_b32 s63, s28
	s_bitset1_b32 s29, 3
.Lcv2_n3:
	s_bitcmp1_b32 s29, 4
	s_cbranch_scc0 .Lcv2_t4
	s_sub_u32 s0, s28, s64
	s_cmp_lt_u32 s0, 60
	s_cbranch_scc1 .Lcv2_slow4
	s_waitcnt vmcnt(60)
.Lcv2_go4:
	v_pk_mul_f32 v[188:189], v[188:189], s[30:31] op_sel_hi:[1,0]
	v_pk_mul_f32 v[190:191], v[190:191], s[30:31] op_sel_hi:[1,0]
	v_pk_mul_f32 v[192:193], v[192:193], s[30:31] op_sel_hi:[1,0]
	v_pk_mul_f32 v[194:195], v[194:195], s[30:31] op_sel_hi:[1,0]
	v_pk_mul_f32 v[196:197], v[196:197], s[30:31] op_sel_hi:[1,0]
	v_pk_mul_f32 v[198:199], v[198:199], s[30:31] op_sel_hi:[1,0]
	v_pk_mul_f32 v[200:201], v[200:201], s[30:31] op_sel_hi:[1,0]
	v_pk_mul_f32 v[202:203], v[202:203], s[30:31] op_sel_hi:[1,0]
	v_pk_mul_f32 v[204:205], v[204:205], s[30:31] op_sel_hi:[1,0]
	v_pk_mul_f32 v[206:207], v[206:207], s[30:31] op_sel_hi:[1,0]
	v_pk_mul_f32 v[208:209], v[208:209], s[30:31] op_sel_hi:[1,0]
	v_pk_mul_f32 v[210:211], v[210:211], s[30:31] op_sel_hi:[1,0]
	v_pk_mul_f32 v[212:213], v[212:213], s[30:31] op_sel_hi:[1,0]
	v_pk_mul_f32 v[214:215], v[214:215], s[30:31] op_sel_hi:[1,0]
	v_pk_mul_f32 v[216:217], v[216:217], s[30:31] op_sel_hi:[1,0]
	v_pk_mul_f32 v[218:219], v[218:219], s[30:31] op_sel_hi:[1,0]
	v_cvt_pk_fp8_f32 v172, v188, v192
	v_cvt_pk_fp8_f32 v174, v189, v193
	v_cvt_pk_fp8_f32 v173, v204, v208
	v_cvt_pk_fp8_f32 v175, v205, v209
	v_cvt_pk_fp8_f32 v172, v196, v200 op_sel:[0,0,1]
	v_cvt_pk_fp8_f32 v174, v197, v201 op_sel:[0,0,1]
	v_cvt_pk_fp8_f32 v173, v212, v216 op_sel:[0,0,1]
	v_cvt_pk_fp8_f32 v175, v213, v217 op_sel:[0,0,1]
	v_cvt_pk_fp8_f32 v176, v190, v194
	v_cvt_pk_fp8_f32 v178, v191, v195
	v_cvt_pk_fp8_f32 v177, v206, v210
	v_cvt_pk_fp8_f32 v179, v207, v211
	v_cvt_pk_fp8_f32 v176, v198, v202 op_sel:[0,0,1]
	v_cvt_pk_fp8_f32 v178, v199, v203 op_sel:[0,0,1]
	v_cvt_pk_fp8_f32 v177, v214, v218 op_sel:[0,0,1]
	v_cvt_pk_fp8_f32 v179, v215, v219 op_sel:[0,0,1]
	s_add_u32 s28, s28, 4
	s_bitset0_b32 s29, 4
	global_store_dwordx2 v140, v[172:173], s[92:93] nt
	global_store_dwordx2 v140, v[174:175], s[92:93] offset:1024 nt
	global_store_dwordx2 v140, v[176:177], s[92:93] offset:2048 nt
	global_store_dwordx2 v140, v[178:179], s[92:93] offset:3072 nt
.Lcv2_t4:
	s_bitcmp1_b32 s29, 31
	s_cbranch_scc1 .Lcv2_n4
	s_mov_b64 exec, s[4:5]
	ds_add_rtn_u32 v2, v141, v187
	s_mov_b64 exec, -1
	s_waitcnt lgkmcnt(0)
	v_readfirstlane_b32 s0, v2
	s_cmp_ge_i32 s0, s9
	s_cbranch_scc1 .Lcv2_e4
	s_add_i32 s0, s22, s0
	s_min_i32 s0, s0, 0xbfff
	s_lshr_b32 s1, s0, 9
	s_mul_i32 s6, s1, 0xab
	s_lshr_b32 s6, s6, 9
	s_mul_i32 s7, s6, 3
	s_sub_i32 s1, s1, s7
	s_and_b32 s0, s0, 0x1ff
	s_lshr_b32 s7, s0, 5
	s_and_b32 s0, s0, 31
	s_lshl_b32 s8, s6, 22
	s_lshl_b32 s10, s7, 18
	s_add_u32 s8, s8, s10
	s_lshl_b32 s10, s0, 7
	s_add_u32 s8, s8, s10
	s_cmp_eq_u32 s1, 0
	s_cselect_b64 s[10:11], s[44:45], s[48:49]
	s_cmp_eq_u32 s1, 2
	s_cselect_b64 s[10:11], s[52:53], s[10:11]
	s_add_u32 s10, s10, s8
	s_addc_u32 s11, s11, 0
	s_lshl_b32 s7, s7, 6
	s_lshl_b32 s8, s6, 20
	s_lshl_b32 s15, s0, 15
	s_add_u32 s8, s8, s15
	s_lshl_b32 s6, s6, 21
	s_lshr_b32 s15, s0, 2
	s_lshl_b32 s15, s15, 18
	s_add_u32 s6, s6, s15
	s_lshl_b32 s15, s1, 17
	s_add_u32 s6, s6, s15
	s_and_b32 s15, s0, 3
	s_lshl_b32 s15, s15, 15
	s_add_u32 s6, s6, s15
	s_cmp_eq_u32 s1, 2
	s_cselect_b32 s6, s8, s6
	s_cselect_b64 s[92:93], s[66:67], s[2:3]
	s_add_u32 s6, s6, s7
	s_add_u32 s92, s92, s6
	s_addc_u32 s93, s93, 0
	global_load_dwordx4 v[188:191], v132, s[10:11] nt
	global_load_dwordx4 v[192:195], v133, s[10:11] nt
	global_load_dwordx4 v[196:199], v134, s[10:11] nt
	global_load_dwordx4 v[200:203], v135, s[10:11] nt
	global_load_dwordx4 v[204:207], v136, s[10:11] nt
	global_load_dwordx4 v[208:211], v137, s[10:11] nt
	global_load_dwordx4 v[212:215], v138, s[10:11] nt
	global_load_dwordx4 v[216:219], v139, s[10:11] nt
	s_add_u32 s28, s28, 8
	s_mov_b32 s64, s28
	s_bitset1_b32 s29, 4
.Lcv2_n4:
	s_bitcmp1_b32 s29, 5
	s_cbranch_scc0 .Lcv2_t5
	s_sub_u32 s0, s28, s65
	s_cmp_lt_u32 s0, 60
	s_cbranch_scc1 .Lcv2_slow5
	s_waitcnt vmcnt(60)
.Lcv2_go5:
	v_pk_mul_f32 v[220:221], v[220:221], s[30:31] op_sel_hi:[1,0]
	v_pk_mul_f32 v[222:223], v[222:223], s[30:31] op_sel_hi:[1,0]
	v_pk_mul_f32 v[224:225], v[224:225], s[30:31] op_sel_hi:[1,0]
	v_pk_mul_f32 v[226:227], v[226:227], s[30:31] op_sel_hi:[1,0]
	v_pk_mul_f32 v[228:229], v[228:229], s[30:31] op_sel_hi:[1,0]
	v_pk_mul_f32 v[230:231], v[230:231], s[30:31] op_sel_hi:[1,0]
	v_pk_mul_f32 v[232:233], v[232:233], s[30:31] op_sel_hi:[1,0]
	v_pk_mul_f32 v[234:235], v[234:235], s[30:31] op_sel_hi:[1,0]
	v_pk_mul_f32 v[236:237], v[236:237], s[30:31] op_sel_hi:[1,0]
	v_pk_mul_f32 v[238:239], v[238:239], s[30:31] op_sel_hi:[1,0]
	v_pk_mul_f32 v[240:241], v[240:241], s[30:31] op_sel_hi:[1,0]
	v_pk_mul_f32 v[242:243], v[242:243], s[30:31] op_sel_hi:[1,0]
	v_pk_mul_f32 v[244:245], v[244:245], s[30:31] op_sel_hi:[1,0]
	v_pk_mul_f32 v[246:247], v[246:247], s[30:31] op_sel_hi:[1,0]
	v_pk_mul_f32 v[248:249], v[248:249], s[30:31] op_sel_hi:[1,0]
	v_pk_mul_f32 v[250:251], v[250:251], s[30:31] op_sel_hi:[1,0]
	v_cvt_pk_fp8_f32 v172, v220, v224
	v_cvt_pk_fp8_f32 v174, v221, v225
	v_cvt_pk_fp8_f32 v173, v236, v240
	v_cvt_pk_fp8_f32 v175, v237, v241
	v_cvt_pk_fp8_f32 v172, v228, v232 op_sel:[0,0,1]
	v_cvt_pk_fp8_f32 v174, v229, v233 op_sel:[0,0,1]
	v_cvt_pk_fp8_f32 v173, v244, v248 op_sel:[0,0,1]
	v_cvt_pk_fp8_f32 v175, v245, v249 op_sel:[0,0,1]
	v_cvt_pk_fp8_f32 v176, v222, v226
	v_cvt_pk_fp8_f32 v178, v223, v227
	v_cvt_pk_fp8_f32 v177, v238, v242
	v_cvt_pk_fp8_f32 v179, v239, v243
	v_cvt_pk_fp8_f32 v176, v230, v234 op_sel:[0,0,1]
	v_cvt_pk_fp8_f32 v178, v231, v235 op_sel:[0,0,1]
	v_cvt_pk_fp8_f32 v177, v246, v250 op_sel:[0,0,1]
	v_cvt_pk_fp8_f32 v179, v247, v251 op_sel:[0,0,1]
	s_add_u32 s28, s28, 4
	s_bitset0_b32 s29, 5
	global_store_dwordx2 v140, v[172:173], s[94:95] nt
	global_store_dwordx2 v140, v[174:175], s[94:95] offset:1024 nt
	global_store_dwordx2 v140, v[176:177], s[94:95] offset:2048 nt
	global_store_dwordx2 v140, v[178:179], s[94:95] offset:3072 nt
.Lcv2_t5:
	s_bitcmp1_b32 s29, 31
	s_cbranch_scc1 .Lcv2_n5
	s_mov_b64 exec, s[4:5]
	ds_add_rtn_u32 v2, v141, v187
	s_mov_b64 exec, -1
	s_waitcnt lgkmcnt(0)
	v_readfirstlane_b32 s0, v2
	s_cmp_ge_i32 s0, s9
	s_cbranch_scc1 .Lcv2_e5
	s_add_i32 s0, s22, s0
	s_min_i32 s0, s0, 0xbfff
	s_lshr_b32 s1, s0, 9
	s_mul_i32 s6, s1, 0xab
	s_lshr_b32 s6, s6, 9
	s_mul_i32 s7, s6, 3
	s_sub_i32 s1, s1, s7
	s_and_b32 s0, s0, 0x1ff
	s_lshr_b32 s7, s0, 5
	s_and_b32 s0, s0, 31
	s_lshl_b32 s8, s6, 22
	s_lshl_b32 s10, s7, 18
	s_add_u32 s8, s8, s10
	s_lshl_b32 s10, s0, 7
	s_add_u32 s8, s8, s10
	s_cmp_eq_u32 s1, 0
	s_cselect_b64 s[10:11], s[44:45], s[48:49]
	s_cmp_eq_u32 s1, 2
	s_cselect_b64 s[10:11], s[52:53], s[10:11]
	s_add_u32 s10, s10, s8
	s_addc_u32 s11, s11, 0
	s_lshl_b32 s7, s7, 6
	s_lshl_b32 s8, s6, 20
	s_lshl_b32 s15, s0, 15
	s_add_u32 s8, s8, s15
	s_lshl_b32 s6, s6, 21
	s_lshr_b32 s15, s0, 2
	s_lshl_b32 s15, s15, 18
	s_add_u32 s6, s6, s15
	s_lshl_b32 s15, s1, 17
	s_add_u32 s6, s6, s15
	s_and_b32 s15, s0, 3
	s_lshl_b32 s15, s15, 15
	s_add_u32 s6, s6, s15
	s_cmp_eq_u32 s1, 2
	s_cselect_b32 s6, s8, s6
	s_cselect_b64 s[94:95], s[66:67], s[2:3]
	s_add_u32 s6, s6, s7
	s_add_u32 s94, s94, s6
	s_addc_u32 s95, s95, 0
	global_load_dwordx4 v[220:223], v132, s[10:11] nt
	global_load_dwordx4 v[224:227], v133, s[10:11] nt
	global_load_dwordx4 v[228:231], v134, s[10:11] nt
	global_load_dwordx4 v[232:235], v135, s[10:11] nt
	global_load_dwordx4 v[236:239], v136, s[10:11] nt
	global_load_dwordx4 v[240:243], v137, s[10:11] nt
	global_load_dwordx4 v[244:247], v138, s[10:11] nt
	global_load_dwordx4 v[248:251], v139, s[10:11] nt
	s_add_u32 s28, s28, 8
	s_mov_b32 s65, s28
	s_bitset1_b32 s29, 5
.Lcv2_n5:
	s_and_b32 s0, s29, 0x7fffffff
	s_cmp_lg_u32 s0, 0
	s_cbranch_scc1 .Lcv2_loop
	s_branch .Lcv2_done
.Lcv2_e0:
	s_bitset1_b32 s29, 31
	s_branch .Lcv2_n0
.Lcv2_slow0:
	s_cmp_lt_u32 s0, 52
	s_cbranch_scc1 .Lcv2_slow0_0
	s_waitcnt vmcnt(52)
	s_branch .Lcv2_go0
.Lcv2_slow0_0:
	s_cmp_lt_u32 s0, 44
	s_cbranch_scc1 .Lcv2_slow0_1
	s_waitcnt vmcnt(44)
	s_branch .Lcv2_go0
.Lcv2_slow0_1:
	s_cmp_lt_u32 s0, 36
	s_cbranch_scc1 .Lcv2_slow0_2
	s_waitcnt vmcnt(36)
	s_branch .Lcv2_go0
.Lcv2_slow0_2:
	s_cmp_lt_u32 s0, 24
	s_cbranch_scc1 .Lcv2_slow0_3
	s_waitcnt vmcnt(24)
	s_branch .Lcv2_go0
.Lcv2_slow0_3:
	s_cmp_lt_u32 s0, 12
	s_cbranch_scc1 .Lcv2_slow0_4
	s_waitcnt vmcnt(12)
	s_branch .Lcv2_go0
.Lcv2_slow0_4:
	s_waitcnt vmcnt(0)
	s_branch .Lcv2_go0

.Lcv2_done:
.LBB0_633:
	s_mov_b64 s[0:1], 0

.LBB0_639:
	s_or_b64 exec, exec, s[0:1]
	v_readfirstlane_b32 s6, v2
	s_cmp_ge_i32 s6, s79
	s_mov_b64 s[0:1], 0
	s_cbranch_scc1 .LBB0_435
	s_cmp_lt_i32 s6, s35
	v_readlane_b32 s0, v255, 58
	v_readlane_b32 s1, v255, 57
	s_cselect_b32 s68, s1, s0
	s_add_i32 s68, s68, s6
	s_cmp_ge_i32 s6, s35
	s_cbranch_scc0 .LBB0_744
	s_cmpk_lt_i32 s68, 0x1000
	s_cselect_b64 s[0:1], -1, 0
	s_cbranch_execz .LBB0_745
	s_branch .LBB0_746
.LBB0_743:
	s_mov_b64 s[88:89], 0
	s_or_b64 s[0:1], s[88:89], s[90:91]
	s_andn2_b64 vcc, exec, s[0:1]
	s_cbranch_vccz .LBB0_436
	s_branch .LBB0_418
